# conversion slices skip the weight-scale table re-read when the launch began at phase 0 (table still in its LDS slot); ffn gate-up and qkv phases: scale reciprocal computed behind the first tile loads
# speedup vs baseline: 1.0031x; 1.0031x over previous
.LBB0_314:
	v_mov_b32_e32 v2, v0
	s_nop 0
	v_cmp_gt_i32_e32 vcc, 6, v2
	v_readlane_b32 s98, v254, 51
	s_cmp_lt_i32 s98, 1
	s_cbranch_scc1 .Lcvw0
	s_and_saveexec_b64 s[0:1], vcc
	s_cbranch_execz .LBB0_316
	v_readlane_b32 s2, v254, 45
	v_ashrrev_i32_e32 v3, 31, v2
	v_readlane_b32 s3, v254, 46
	s_nop 1
	v_lshl_add_u64 v[4:5], v[2:3], 2, s[2:3]
	global_load_dword v1, v[4:5], off sc1
	v_lshl_add_u32 v3, v2, 2, 0
	v_add_u32_e32 v3, 0x23000, v3
	s_waitcnt vmcnt(0)
	ds_write_b32 v3, v1

.Lcvw0:
	v_readlane_b32 s0, v254, 7
	s_lshl_b32 s47, s0, 3
	v_readlane_b32 s0, v254, 44
	s_add_i32 s48, s0, 0x2000
	s_add_i32 s24, s48, s47
	s_cmp_gt_i32 s24, 0xa7ff
	s_waitcnt vmcnt(0) lgkmcnt(0)
	s_barrier
	s_cbranch_scc1 .LBB0_581
	s_cmpk_gt_i32 s24, 0x17ff
	s_cbranch_scc0 .LBB0_325
	s_cmpk_gt_u32 s24, 0x1fff
	s_cbranch_scc0 .LBB0_328
	s_cmpk_gt_u32 s24, 0x35ff
	s_cbranch_scc0 .LBB0_329
	s_cmpk_gt_u32 s24, 0x4bff
	s_cbranch_scc0 .LBB0_330
	s_cmpk_gt_u32 s24, 0x61ff
	s_cbranch_scc0 .LBB0_331
	s_cmpk_gt_u32 s24, 0x79ff
	s_cbranch_scc0 .LBB0_332
	s_cmpk_gt_u32 s24, 0x81ff
	s_cbranch_scc0 .LBB0_333
	s_add_i32 s0, s24, 0x7e00
	s_and_b32 s1, s0, 0xffff
	s_add_i32 s2, s24, 0x6200
	s_cmpk_lt_u32 s1, 0x1c00
	s_cselect_b32 s0, s0, s2
	s_bfe_u32 s2, s0, 0xc0004
	s_mulk_i32 s2, 0x2493
	s_lshr_b32 s3, s2, 16
	s_mul_i32 s2, s3, 0x70
	s_sub_i32 s12, s0, s2
	s_lshl_b32 s13, s12, 6
	s_and_b32 s2, s13, 0xffc0
	s_cmpk_gt_u32 s1, 0x1bff
	s_cselect_b32 s0, 0x3800000, 0
	s_cselect_b32 s14, 0x1c00000, 0
	s_add_u32 s10, s64, s0
	s_addc_u32 s11, s65, 0
	s_add_u32 s0, s96, 0x8a00000
	s_addc_u32 s1, s97, 0
	s_lshl_b32 s12, s12, 7
	s_and_b32 s12, s12, 0x3f00
	s_and_b32 s13, s13, 64
	s_mov_b32 s15, 0
	s_or_b32 s25, s12, s13
	s_mov_b64 s[12:13], 0
	s_branch .LBB0_334

.Lcvw1:
	v_readlane_b32 s0, v254, 7
	s_lshl_b32 s46, s0, 3
	v_readlane_b32 s0, v254, 44
	s_add_i32 s47, s0, 0xa800
	s_add_i32 s20, s47, s46
	s_cmp_gt_i32 s20, 0xffff
	s_waitcnt lgkmcnt(0)
	s_barrier
	s_cbranch_scc1 .LBB0_1032
	s_cmpk_gt_i32 s20, 0x17ff
	s_cbranch_scc0 .LBB0_776
	s_cmpk_gt_u32 s20, 0x1fff
	s_cbranch_scc0 .LBB0_779
	s_cmpk_gt_u32 s20, 0x35ff
	s_cbranch_scc0 .LBB0_780
	s_cmpk_gt_u32 s20, 0x4bff
	s_cbranch_scc0 .LBB0_781
	s_cmpk_gt_u32 s20, 0x61ff
	s_cbranch_scc0 .LBB0_782
	s_cmpk_gt_u32 s20, 0x79ff
	s_cbranch_scc0 .LBB0_783
	s_cmpk_gt_u32 s20, 0x81ff
	s_cbranch_scc0 .LBB0_784
	s_add_i32 s0, s20, 0x7e00
	s_bfe_u32 s1, s0, 0x6000a
	s_mulk_i32 s1, 0x2493
	s_lshr_b32 s8, s1, 16
	s_mul_i32 s1, s8, 0x1c00
	s_sub_i32 s0, s0, s1
	s_bfe_u32 s1, s0, 0xc0004
	s_mulk_i32 s1, 0x2493
	s_lshr_b32 s3, s1, 16
	s_mul_i32 s1, s3, 0x70
	s_sub_i32 s9, s0, s1
	s_lshl_b32 s12, s9, 6
	s_and_b32 s2, s12, 0xffc0
	s_mul_i32 s0, s8, 0x3800000
	s_add_u32 s4, s64, s0
	s_addc_u32 s5, s65, 0
	s_add_u32 s0, s96, 0x8a00000
	s_addc_u32 s1, s97, 0
	s_mul_i32 s10, s8, 0x1c00000
	s_lshl_b32 s8, s9, 7
	s_and_b32 s8, s8, 0x3f00
	s_and_b32 s9, s12, 64
	s_mov_b32 s11, 0
	s_or_b32 s21, s8, s9
	s_mov_b64 s[8:9], 0
	s_branch .LBB0_785

.LBB0_1174:
	s_cmp_lt_i32 s56, 7
	s_cselect_b64 s[0:1], -1, 0
	s_cmp_gt_i32 s57, 6
	s_cselect_b64 s[2:3], -1, 0
	s_and_b64 s[0:1], s[0:1], s[2:3]
	s_andn2_b64 vcc, exec, s[0:1]
	s_cbranch_vccnz .LBB0_1571
	s_waitcnt vmcnt(0)
	v_mov_b32_e32 v1, v0
	s_add_u32 s6, s96, 0x2800000
	v_mov_b32_e32 v1, 0x508000
	global_load_dword v204, v1, s[96:97] offset:4 sc1
	s_nop 0
	global_load_dword v205, v1, s[96:97] offset:8 sc1
	v_and_b32_e32 v3, 32, v0
	v_lshrrev_b32_e32 v4, 5, v0
	v_and_b32_e32 v4, 4, v4
	v_and_b32_e32 v194, 24, v226
	v_or_b32_e32 v207, 0x2000, v249
	s_addc_u32 s7, s97, 0
	v_bitop3_b32 v209, v249, v3, 48 bitop3:0x6c
	v_bfe_u32 v3, v0, 2, 2
	v_bfe_u32 v10, v0, 2, 4
	v_lshrrev_b32_e32 v9, 3, v0
	s_movk_i32 s1, 0x70
	v_or3_b32 v3, v4, v3, v194
	v_lshrrev_b32_e32 v4, 7, v207
	s_add_u32 s33, s96, 0x4aa00000
	v_and_or_b32 v5, v9, 48, v10
	s_movk_i32 s2, 0x60
	v_and_or_b32 v10, v4, s1, v10
	s_addc_u32 s42, s97, 0
	s_and_b32 s1, s86, 7
	v_and_b32_e32 v8, 64, v0
	v_and_or_b32 v9, v9, 32, v3
	v_and_or_b32 v3, v4, s2, v3
	s_mul_i32 s2, s1, 0x651
	v_or_b32_e32 v8, v209, v8
	s_lshr_b32 s43, s2, 10
	s_movk_i32 s0, 0x6010
	v_lshlrev_b32_e32 v4, 8, v8
	s_cmp_eq_u32 s1, 0
	v_bitop3_b32 v4, v4, s0, v249 bitop3:0xc8
	s_cselect_b64 s[0:1], -1, 0
	s_cmpk_gt_i32 s86, 0xaff
	v_lshlrev_b32_e32 v6, 6, v0
	v_lshlrev_b32_e32 v7, 2, v0
	s_cselect_b64 s[2:3], -1, 0
	v_and_b32_e32 v6, 0x3c0, v6
	v_and_b32_e32 v7, 32, v7
	v_lshlrev_b32_e32 v211, 1, v194
	v_lshl_or_b32 v202, v3, 5, v4
	s_or_b64 s[0:1], s[2:3], s[0:1]
	v_bitop3_b32 v213, v211, v7, v6 bitop3:0x36
	v_lshl_or_b32 v196, v5, 11, v8
	v_lshl_or_b32 v200, v9, 5, v4
	v_lshl_or_b32 v198, v10, 11, v8
	s_and_b64 s[0:1], exec, s[0:1]
	v_readfirstlane_b32 s8, v0
	s_mov_b64 vcc, s[0:1]
	s_cbranch_vccnz .Lp6_div
	s_ashr_i32 s35, s86, 31
	s_lshr_b32 s0, s35, 29
	s_add_i32 s0, s86, s0
	s_lshr_b32 s2, s8, 6
	s_and_b32 s1, s0, -8
	s_lshr_b32 s5, s8, 8
	s_lshl_b32 s34, s2, 10
	s_sub_i32 s1, s86, s1
	s_cmp_lt_i32 s1, 0
	s_movk_i32 s36, 0x161
	s_cselect_b32 s3, s36, 0x160
	s_mul_i32 s1, s1, s3
	s_ashr_i32 s0, s0, 3
	s_add_i32 s1, s1, s0
	s_mul_hi_i32 s0, s1, 0x2e8ba2e9
	s_lshr_b32 s3, s0, 31
	s_ashr_i32 s0, s0, 5
	s_add_i32 s0, s0, s3
	s_lshl_b32 s3, s0, 2
	s_mulk_i32 s0, 0xb0
	s_sub_i32 s0, s1, s0
	s_bfe_u32 s1, s0, 0x2001d
	s_add_i32 s1, s0, s1
	s_and_b32 s4, s1, 0xfffc
	s_sub_i32 s0, s0, s4
	s_sext_i32_i16 s0, s0
	s_add_i32 s18, s3, s0
	s_sext_i32_i16 s0, s1
	s_lshr_b32 s4, s0, 2
	s_ashr_i32 s19, s18, 31
	s_bfe_i64 s[10:11], s[4:5], 0x100000
	s_lshl_b64 s[0:1], s[18:19], 19
	s_lshl_b64 s[10:11], s[10:11], 19
	s_add_u32 s24, s6, s10
	s_addc_u32 s25, s7, s11
	s_add_i32 s37, s34, 0
	s_add_i32 s38, s37, 0x10000
	s_add_i32 s39, s37, 0x12000
	s_mov_b32 m0, s38
	s_add_u32 s10, s24, 0x1000
	global_load_lds_dwordx4 v200, s[24:25]
	s_mov_b32 m0, s39
	s_addc_u32 s11, s25, 0
	s_add_i32 s40, s37, 0x14000
	global_load_lds_dwordx4 v202, s[24:25]
	s_mov_b32 m0, s40
	s_add_i32 s41, s37, 0x16000
	global_load_lds_dwordx4 v200, s[10:11]
	s_mov_b32 m0, s41
	v_mov_b32_e32 v201, 0
	global_load_lds_dwordx4 v202, s[10:11]
	v_readlane_b32 s10, v254, 49
	v_readlane_b32 s11, v254, 50
	s_add_u32 s20, s10, s0
	s_addc_u32 s21, s11, s1
	s_add_i32 s45, s37, 0x2000
	s_mov_b32 m0, s37
	s_add_u32 s0, s20, 0x40000
	global_load_lds_dwordx4 v196, s[20:21]
	s_mov_b32 m0, s45
	s_addc_u32 s1, s21, 0
	s_add_i32 s46, s37, 0x4000
	global_load_lds_dwordx4 v198, s[20:21]
	s_mov_b32 m0, s46
	s_add_i32 s47, s37, 0x6000
	global_load_lds_dwordx4 v196, s[0:1]
	s_mov_b32 m0, s47
	v_mov_b32_e32 v197, v201
	global_load_lds_dwordx4 v198, s[0:1]
	s_waitcnt vmcnt(9)
	v_div_scale_f32 v3, s[98:99], v204, v204, 1.0
	s_waitcnt vmcnt(8)
	v_div_scale_f32 v5, s[98:99], v205, v205, 1.0
	v_rcp_f32_e32 v6, v3
	v_rcp_f32_e32 v7, v5
	v_div_scale_f32 v4, vcc, 1.0, v204, 1.0
	v_fma_f32 v9, -v3, v6, 1.0
	v_fma_f32 v10, -v5, v7, 1.0
	v_fmac_f32_e32 v6, v9, v6
	v_div_scale_f32 v8, s[100:101], 1.0, v205, 1.0
	v_fmac_f32_e32 v7, v10, v7
	v_mul_f32_e32 v9, v4, v6
	v_mul_f32_e32 v10, v8, v7
	v_fma_f32 v11, -v3, v9, v4
	v_fma_f32 v12, -v5, v10, v8
	v_fmac_f32_e32 v9, v11, v6
	v_fmac_f32_e32 v10, v12, v7
	v_fma_f32 v3, -v3, v9, v4
	v_fma_f32 v4, -v5, v10, v8
	v_div_fmas_f32 v3, v3, v6, v9
	s_mov_b64 vcc, s[100:101]
	v_div_fixup_f32 v204, v3, v204, 1.0
	v_div_fmas_f32 v2, v4, v7, v10
	v_div_fixup_f32 v205, v2, v205, 1.0
	v_mov_b32_e32 v199, v201
	s_cmp_eq_u32 s5, 1
	v_mov_b32_e32 v203, v201
	v_lshl_add_u64 v[2:3], s[20:21], 0, v[196:197]
	s_cselect_b64 s[0:1], -1, 0
	s_cmp_lg_u32 s5, 1
	v_lshl_add_u64 v[4:5], s[20:21], 0, v[198:199]
	s_cbranch_scc1 .LBB0_1178
	s_barrier

.LBB0_1201:
	s_andn2_b64 vcc, exec, s[14:15]
	s_cbranch_vccnz .LBB0_1179
	s_waitcnt vmcnt(0)
	v_lshrrev_b32_e32 v226, 1, v0
	s_barrier
	s_branch .LBB0_1204
	s_branch .LBB0_1203
.Lp6_div:
	s_waitcnt vmcnt(1)
	v_div_scale_f32 v3, s[98:99], v204, v204, 1.0
	s_waitcnt vmcnt(0)
	v_div_scale_f32 v5, s[98:99], v205, v205, 1.0
	v_rcp_f32_e32 v6, v3
	v_rcp_f32_e32 v7, v5
	v_div_scale_f32 v4, vcc, 1.0, v204, 1.0
	v_fma_f32 v9, -v3, v6, 1.0
	v_fma_f32 v10, -v5, v7, 1.0
	v_fmac_f32_e32 v6, v9, v6
	v_div_scale_f32 v8, s[100:101], 1.0, v205, 1.0
	v_fmac_f32_e32 v7, v10, v7
	v_mul_f32_e32 v9, v4, v6
	v_mul_f32_e32 v10, v8, v7
	v_fma_f32 v11, -v3, v9, v4
	v_fma_f32 v12, -v5, v10, v8
	v_fmac_f32_e32 v9, v11, v6
	v_fmac_f32_e32 v10, v12, v7
	v_fma_f32 v3, -v3, v9, v4
	v_fma_f32 v4, -v5, v10, v8
	v_div_fmas_f32 v3, v3, v6, v9
	s_mov_b64 vcc, s[100:101]
	v_div_fixup_f32 v204, v3, v204, 1.0
	v_div_fmas_f32 v2, v4, v7, v10
	v_div_fixup_f32 v205, v2, v205, 1.0

.Lcvw2:
	v_readlane_b32 s0, v254, 7
	s_lshl_b32 s45, s0, 3
	v_readlane_b32 s0, v254, 44
	s_add_i32 s46, s0, 0x10000
	s_add_i32 s20, s46, s45
	s_cmp_gt_i32 s20, 0x1c7ff
	s_waitcnt vmcnt(0) lgkmcnt(0)
	s_barrier
	s_cbranch_scc1 .LBB0_1493
	s_cmpk_gt_i32 s20, 0x17ff
	s_cbranch_scc0 .LBB0_1216
	s_cmpk_gt_u32 s20, 0x1fff
	s_cbranch_scc0 .LBB0_1219
	s_cmpk_gt_u32 s20, 0x35ff
	s_cbranch_scc0 .LBB0_1220
	s_cmpk_gt_u32 s20, 0x4bff
	s_cbranch_scc0 .LBB0_1221
	s_cmpk_gt_u32 s20, 0x61ff
	s_cbranch_scc0 .LBB0_1222
	s_cmpk_gt_u32 s20, 0x79ff
	s_cbranch_scc0 .LBB0_1223
	s_cmpk_gt_u32 s20, 0x81ff
	s_cbranch_scc0 .LBB0_1224
	s_add_u32 s0, s96, 0x8a00000
	s_addc_u32 s1, s97, 0
	s_cmp_gt_u32 s20, 0x161ff
	s_cbranch_scc0 .LBB0_1225
	s_add_i32 s2, s20, 0x9e00
	s_bfe_u32 s3, s2, 0x6000a
	s_mulk_i32 s3, 0x2493
	s_lshr_b32 s8, s3, 16
	s_mul_i32 s3, s8, 0x1c00
	s_sub_i32 s2, s2, s3
	s_bfe_u32 s3, s2, 0xc0004
	s_mulk_i32 s3, 0x2493
	s_lshr_b32 s3, s3, 16
	s_mul_i32 s4, s3, 0x70
	s_sub_i32 s2, s2, s4
	s_lshl_b32 s10, s2, 6
	s_and_b32 s2, s10, 0xffc0
	s_mul_i32 s4, s8, 0x3800000
	s_add_u32 s4, s66, s4
	s_addc_u32 s5, s67, 0
	s_lshl_b32 s11, s2, 1
	s_and_b32 s10, s10, 64
	s_or_b32 s10, s11, s10
	s_mov_b32 s9, 0
	s_mul_i32 s8, s8, 0x1c00000
	s_or_b32 s21, s10, 0x80
	s_mov_b64 s[10:11], 0
	s_branch .LBB0_1226

.Lcvw3:
	v_readlane_b32 s0, v254, 7
	s_lshl_b32 s48, s0, 3
	v_readlane_b32 s0, v254, 44
	s_add_i32 s49, s0, 0x1c800
	s_add_i32 s20, s49, s48
	s_cmp_gt_i32 s20, 0x24fff
	s_waitcnt lgkmcnt(0)
	s_barrier
	s_cbranch_scc1 .LBB0_1919
	s_cmpk_gt_i32 s20, 0x17ff
	s_cbranch_scc0 .LBB0_1615
	s_cmpk_gt_u32 s20, 0x1fff
	s_cbranch_scc0 .LBB0_1618
	s_cmpk_gt_u32 s20, 0x35ff
	s_cbranch_scc0 .LBB0_1619
	s_cmpk_gt_u32 s20, 0x4bff
	s_cbranch_scc0 .LBB0_1620
	s_cmpk_gt_u32 s20, 0x61ff
	s_cbranch_scc0 .LBB0_1621
	s_cmpk_gt_u32 s20, 0x79ff
	s_cbranch_scc0 .LBB0_1622
	s_cmpk_gt_u32 s20, 0x81ff
	s_cbranch_scc0 .LBB0_1623
	s_cmp_gt_u32 s20, 0x161ff
	s_cbranch_scc0 .LBB0_1624
	s_cmp_gt_u32 s20, 0x241ff
	s_mov_b64 s[14:15], -1
	s_cbranch_scc0 .LBB0_1625
	s_add_i32 s0, s20, 0xbe00
	s_bfe_u32 s1, s0, 0x6000a
	s_mulk_i32 s1, 0x2493
	s_lshr_b32 s8, s1, 16
	s_mul_i32 s1, s8, 0x1c00
	s_sub_i32 s0, s0, s1
	s_and_b32 s1, s0, 0xffff
	s_bfe_u32 s3, s0, 0xb0005
	s_lshl_b32 s0, s1, 6
	s_and_b32 s2, s0, 0x7c0
	s_mul_i32 s0, s8, 0x3800000
	v_readlane_b32 s16, v254, 0
	v_readlane_b32 s17, v254, 1
	s_add_u32 s4, s16, s0
	s_addc_u32 s5, s17, 0
	s_add_u32 s0, s96, 0x24a00000
	s_mov_b32 s11, 0
	v_readlane_b32 s18, v254, 2
	v_readlane_b32 s19, v254, 3
	s_addc_u32 s1, s97, 0
	s_mul_i32 s10, s8, 0xe00000
	s_mov_b64 s[8:9], 0
	s_branch .LBB0_1626

.LBB0_2066:
	s_add_u32 s0, s96, 0x300000
	s_addc_u32 s1, s97, 0
	v_writelane_b32 v255, s0, 7
	s_cmp_lt_i32 s56, 10
	s_nop 0
	v_writelane_b32 v255, s1, 8
	s_cselect_b64 s[0:1], -1, 0
	s_cmp_gt_i32 s57, 9
	s_cselect_b64 s[2:3], -1, 0
	s_and_b64 s[0:1], s[0:1], s[2:3]
	s_andn2_b64 vcc, exec, s[0:1]
	s_cbranch_vccnz .LBB0_2639
	s_waitcnt vmcnt(0)
	v_mov_b32_e32 v1, v0
	s_and_b32 s3, s86, 7
	v_mov_b32_e32 v1, 0x508000
	global_load_dword v218, v1, s[96:97] offset:12 sc1
	s_cmp_gt_u32 s3, 1
	s_cselect_b64 s[0:1], -1, 0
	s_cmpk_lt_i32 s86, 0x600
	s_cselect_b64 s[4:5], -1, 0
	s_and_b64 s[4:5], s[4:5], s[0:1]
	v_cndmask_b32_e64 v2, 0, 1, s[4:5]
	v_cmp_ne_u32_e64 s[0:1], 1, v2
	s_andn2_b64 vcc, exec, s[4:5]
	v_readfirstlane_b32 s2, v0
	s_cbranch_vccnz .LBB0_2069
	s_ashr_i32 s4, s86, 31
	s_lshr_b32 s4, s4, 29
	s_add_i32 s4, s86, s4
	s_and_b32 s5, s4, -8
	s_sub_i32 s5, s86, s5
	s_cmp_lt_i32 s5, 0
	s_movk_i32 s6, 0xc1
	s_cselect_b32 s6, s6, 0xc0
	s_mul_i32 s5, s5, s6
	s_ashr_i32 s4, s4, 3
	s_add_i32 s5, s5, s4
	s_mul_hi_i32 s4, s5, 0x2aaaaaab
	s_lshr_b32 s6, s4, 31
	s_ashr_i32 s4, s4, 4
	s_add_i32 s4, s4, s6
	s_lshl_b32 s6, s4, 2
	s_mulk_i32 s4, 0x60
	s_sub_i32 s4, s5, s4
	s_bfe_i32 s5, s4, 0x80000
	s_bfe_u32 s5, s5, 0x2000d
	s_add_i32 s5, s4, s5
	s_and_b32 s7, s5, 0xfc
	s_sub_i32 s4, s4, s7
	s_sext_i32_i8 s4, s4
	s_add_i32 s30, s6, s4
	s_bfe_i32 s4, s5, 0x80000
	s_sext_i32_i16 s4, s4
	s_ashr_i32 s28, s4, 2
.LBB0_2069:
	s_add_u32 s4, s96, 0x6a00000
	s_addc_u32 s5, s97, 0
	s_add_u32 s6, s96, 0x3ea00000
	v_and_b32_e32 v1, 32, v0
	v_bitop3_b32 v230, v249, v1, 48 bitop3:0x6c
	v_and_b32_e32 v1, 64, v0
	v_lshrrev_b32_e32 v3, 5, v0
	s_mulk_i32 s3, 0xde
	v_or_b32_e32 v1, v230, v1
	v_and_b32_e32 v2, 24, v226
	v_and_b32_e32 v3, 4, v3
	v_bfe_u32 v4, v0, 2, 2
	v_bfe_u32 v6, v0, 2, 4
	v_lshrrev_b32_e32 v5, 3, v0
	s_addc_u32 s7, s97, 0
	s_bfe_u32 s33, s3, 0x80008
	v_or3_b32 v2, v3, v4, v2
	v_lshlrev_b32_e32 v3, 8, v1
	s_movk_i32 s3, 0x6010
	v_and_or_b32 v4, v5, 48, v6
	v_or_b32_e32 v231, 0x2000, v249
	v_bitop3_b32 v3, v3, s3, v249 bitop3:0xc8
	v_and_or_b32 v5, v5, 32, v2
	v_lshl_or_b32 v194, v4, 11, v1
	v_lshrrev_b32_e32 v4, 7, v231
	s_movk_i32 s3, 0x70
	v_lshl_or_b32 v196, v5, 5, v3
	v_and_or_b32 v5, v4, s3, v6
	s_movk_i32 s3, 0x60
	v_and_or_b32 v2, v4, s3, v2
	v_lshl_or_b32 v198, v5, 11, v1
	v_lshl_or_b32 v200, v2, 5, v3
	v_lshlrev_b32_e32 v1, 6, v0
	v_lshlrev_b32_e32 v2, 2, v0
	v_lshlrev_b32_e32 v232, 4, v223
	v_and_b32_e32 v1, 0x3c0, v1
	v_and_b32_e32 v2, 32, v2
	s_add_u32 s8, s96, 0x600000
	s_addc_u32 s9, s97, 0
	s_and_b64 vcc, exec, s[0:1]
	v_bitop3_b32 v233, v232, v2, v1 bitop3:0x36
	s_cbranch_vccnz .Lp9_div
	s_lshr_b32 s12, s2, 6
	s_ashr_i32 s31, s30, 31
	s_ashr_i32 s29, s28, 31
	s_lshr_b32 s16, s2, 8
	s_lshl_b32 s44, s12, 10
	s_lshl_b64 s[0:1], s[30:31], 19
	s_lshl_b64 s[10:11], s[28:29], 19
	s_add_u32 s36, s4, s10
	s_addc_u32 s37, s5, s11
	s_add_i32 s29, s44, 0
	s_add_i32 s31, s29, 0x10000
	s_add_i32 s45, s29, 0x12000
	s_mov_b32 m0, s31
	s_add_u32 s10, s36, 0x1000
	global_load_lds_dwordx4 v196, s[36:37]
	s_mov_b32 m0, s45
	s_addc_u32 s11, s37, 0
	s_add_i32 s46, s29, 0x14000
	global_load_lds_dwordx4 v200, s[36:37]
	s_mov_b32 m0, s46
	s_add_i32 s47, s29, 0x16000
	global_load_lds_dwordx4 v196, s[10:11]
	s_mov_b32 m0, s47
	v_mov_b32_e32 v203, 0
	global_load_lds_dwordx4 v200, s[10:11]
	v_readlane_b32 s10, v254, 49
	v_readlane_b32 s11, v254, 50
	s_add_u32 s0, s10, s0
	s_addc_u32 s1, s11, s1
	s_add_i32 s49, s29, 0x2000
	s_mov_b32 m0, s29
	s_add_u32 s10, s0, 0x40000
	global_load_lds_dwordx4 v194, s[0:1]
	s_mov_b32 m0, s49
	s_addc_u32 s11, s1, 0
	s_add_i32 s50, s29, 0x4000
	global_load_lds_dwordx4 v198, s[0:1]
	s_mov_b32 m0, s50
	s_add_i32 s51, s29, 0x6000
	global_load_lds_dwordx4 v194, s[10:11]
	s_mov_b32 m0, s51
	v_mov_b32_e32 v195, v203
	global_load_lds_dwordx4 v198, s[10:11]
	s_waitcnt vmcnt(8)
	v_div_scale_f32 v2, s[98:99], v218, v218, 1.0
	v_rcp_f32_e32 v3, v2
	s_nop 0
	v_fma_f32 v4, -v2, v3, 1.0
	v_fmac_f32_e32 v3, v4, v3
	v_div_scale_f32 v4, vcc, 1.0, v218, 1.0
	v_mul_f32_e32 v5, v4, v3
	v_fma_f32 v6, -v2, v5, v4
	v_fmac_f32_e32 v5, v6, v3
	v_fma_f32 v2, -v2, v5, v4
	v_div_fmas_f32 v2, v2, v3, v5
	v_div_fixup_f32 v218, v2, v218, 1.0
	v_mov_b32_e32 v199, v203
	s_cmp_eq_u32 s16, 1
	s_mov_b32 s3, 0
	v_mov_b32_e32 v197, v203
	v_mov_b32_e32 v201, v203
	v_lshl_add_u64 v[2:3], s[0:1], 0, v[194:195]
	s_cselect_b64 s[10:11], -1, 0
	s_cmp_lg_u32 s16, 1
	v_lshl_add_u64 v[4:5], s[0:1], 0, v[198:199]
	s_cbranch_scc1 .LBB0_2072
	s_barrier

.LBB0_2168:
	s_waitcnt vmcnt(0)
	v_readlane_b32 s56, v254, 51
	v_readlane_b32 s60, v254, 55
	v_readlane_b32 s57, v254, 52
	v_readlane_b32 s61, v254, 56
	v_readlane_b32 s64, v254, 59
	v_readlane_b32 s65, v254, 60
	v_readlane_b32 s66, v254, 61
	v_readlane_b32 s67, v254, 62
	s_barrier
	v_readlane_b32 s58, v254, 53
	v_readlane_b32 s59, v254, 54
	v_readlane_b32 s62, v254, 57
	v_readlane_b32 s63, v254, 58
	s_branch .LBB0_2170
	s_branch .LBB0_2169
.Lp9_div:
	s_waitcnt vmcnt(0)
	v_div_scale_f32 v2, s[98:99], v218, v218, 1.0
	v_rcp_f32_e32 v3, v2
	s_nop 0
	v_fma_f32 v4, -v2, v3, 1.0
	v_fmac_f32_e32 v3, v4, v3
	v_div_scale_f32 v4, vcc, 1.0, v218, 1.0
	v_mul_f32_e32 v5, v4, v3
	v_fma_f32 v6, -v2, v5, v4
	v_fmac_f32_e32 v5, v6, v3
	v_fma_f32 v2, -v2, v5, v4
	v_div_fmas_f32 v2, v2, v3, v5
	v_div_fixup_f32 v218, v2, v218, 1.0

.Lcvw4:
	v_readlane_b32 s0, v254, 7
	s_lshl_b32 s49, s0, 3
	v_readlane_b32 s0, v254, 44
	s_add_i32 s50, s0, 0x25000
	s_add_i32 s24, s50, s49
	s_cmp_gt_i32 s24, 0x2c1ff
	s_waitcnt vmcnt(0) lgkmcnt(0)
	s_barrier
	s_cbranch_scc1 .LBB0_2487
	s_cmpk_gt_i32 s24, 0x17ff
	s_cbranch_scc0 .LBB0_2183
	s_cmpk_gt_u32 s24, 0x1fff
	s_cbranch_scc0 .LBB0_2186
	s_cmpk_gt_u32 s24, 0x35ff
	s_cbranch_scc0 .LBB0_2187
	s_cmpk_gt_u32 s24, 0x4bff
	s_cbranch_scc0 .LBB0_2188
	s_cmpk_gt_u32 s24, 0x61ff
	s_cbranch_scc0 .LBB0_2189
	s_cmpk_gt_u32 s24, 0x79ff
	s_cbranch_scc0 .LBB0_2190
	s_cmpk_gt_u32 s24, 0x81ff
	s_cbranch_scc0 .LBB0_2191
	s_cmp_gt_u32 s24, 0x161ff
	s_cbranch_scc0 .LBB0_2192
	s_cmp_gt_u32 s24, 0x241ff
	s_mov_b64 s[18:19], -1
	s_cbranch_scc0 .LBB0_2193
	s_add_i32 s0, s24, 0xbe00
	s_bfe_u32 s1, s0, 0x6000a
	s_mulk_i32 s1, 0x2493
	s_lshr_b32 s12, s1, 16
	s_mul_i32 s1, s12, 0x1c00
	s_sub_i32 s0, s0, s1
	s_and_b32 s1, s0, 0xffff
	s_bfe_u32 s3, s0, 0xb0005
	s_lshl_b32 s0, s1, 6
	s_and_b32 s2, s0, 0x7c0
	s_mul_i32 s0, s12, 0x3800000
	v_readlane_b32 s20, v254, 0
	v_readlane_b32 s21, v254, 1
	s_add_u32 s10, s20, s0
	s_addc_u32 s11, s21, 0
	s_add_u32 s0, s96, 0x24a00000
	s_mov_b32 s15, 0
	v_readlane_b32 s22, v254, 2
	v_readlane_b32 s23, v254, 3
	s_addc_u32 s1, s97, 0
	s_mul_i32 s14, s12, 0xe00000
	s_mov_b64 s[12:13], 0
	s_branch .LBB0_2194

.LBB0_2890:
	v_mov_b32_e32 v2, v0
	s_ashr_i32 s95, s94, 31
	s_nop 0
	v_cmp_gt_i32_e32 vcc, 6, v2
	v_readlane_b32 s98, v254, 51
	s_cmp_lt_i32 s98, 1
	s_cbranch_scc1 .Lcvw5
	s_and_saveexec_b64 s[0:1], vcc
	s_cbranch_execz .LBB0_2892
	v_readlane_b32 s2, v254, 45
	v_ashrrev_i32_e32 v3, 31, v2
	v_readlane_b32 s3, v254, 46
	s_nop 1
	v_lshl_add_u64 v[4:5], v[2:3], 2, s[2:3]
	global_load_dword v1, v[4:5], off sc1
	v_lshl_add_u32 v3, v2, 2, 0
	v_add_u32_e32 v3, 0x23000, v3
	s_waitcnt vmcnt(0)
	ds_write_b32 v3, v1

.Lcvw5:
	v_readlane_b32 s0, v254, 7
	s_lshl_b32 s33, s0, 3
	v_readlane_b32 s0, v254, 44
	s_add_i32 s44, s0, 0x2c200
	s_add_i32 s18, s44, s33
	s_cmp_gt_i32 s18, 0x321ff
	s_waitcnt lgkmcnt(0)
	s_barrier
	s_cbranch_scc1 .LBB0_3207
	s_cmpk_gt_i32 s18, 0x17ff
	s_cbranch_scc0 .LBB0_2903
	s_cmpk_gt_u32 s18, 0x1fff
	s_cbranch_scc0 .LBB0_2906
	s_cmpk_gt_u32 s18, 0x35ff
	s_cbranch_scc0 .LBB0_2907
	s_cmpk_gt_u32 s18, 0x4bff
	s_cbranch_scc0 .LBB0_2908
	s_cmpk_gt_u32 s18, 0x61ff
	s_cbranch_scc0 .LBB0_2909
	s_cmpk_gt_u32 s18, 0x79ff
	s_cbranch_scc0 .LBB0_2910
	s_cmpk_gt_u32 s18, 0x81ff
	s_cbranch_scc0 .LBB0_2911
	s_cmp_gt_u32 s18, 0x161ff
	s_cbranch_scc0 .LBB0_2912
	s_cmp_gt_u32 s18, 0x241ff
	s_mov_b64 s[12:13], -1
	s_cbranch_scc0 .LBB0_2913
	s_add_i32 s0, s18, 0xbe00
	s_bfe_u32 s1, s0, 0x6000a
	s_mulk_i32 s1, 0x2493
	s_lshr_b32 s6, s1, 16
	s_mul_i32 s1, s6, 0x1c00
	s_sub_i32 s0, s0, s1
	s_and_b32 s1, s0, 0xffff
	s_bfe_u32 s3, s0, 0xb0005
	s_lshl_b32 s0, s1, 6
	s_and_b32 s2, s0, 0x7c0
	s_mul_i32 s0, s6, 0x3800000
	v_readlane_b32 s20, v254, 0
	v_readlane_b32 s21, v254, 1
	s_add_u32 s4, s20, s0
	s_addc_u32 s5, s21, 0
	s_add_u32 s0, s96, 0x24a00000
	s_mov_b32 s9, 0
	v_readlane_b32 s22, v254, 2
	v_readlane_b32 s23, v254, 3
	s_addc_u32 s1, s97, 0
	s_mul_i32 s8, s6, 0xe00000
	s_mov_b64 s[6:7], 0
	s_branch .LBB0_2914
